# diff units: conversion-group weight loads issued at the start of the unit epilogue
# speedup vs baseline: 1.0114x; 1.0114x over previous
.LBB0_461:
	s_add_i32 s30, s30, 0x8000
	s_add_i32 s22, s22, 1
	s_sub_i32 s23, s23, 64
	s_add_i32 s29, s29, 64
	s_cmp_eq_u32 s31, 0
	s_cbranch_scc0 .LBB0_439
	v_mov_b32_e32 v2, v167
	s_nop 1
	v_permlane32_swap_b32_e32 v167, v2
	v_add_f32_e32 v2, v167, v2
	v_div_scale_f32 v4, s[2:3], v2, v2, 1.0
	v_rcp_f32_e32 v5, v4
	s_cmp_eq_u32 s5, 0
	s_cselect_b64 s[2:3], -1, 0
	s_waitcnt vmcnt(0) lgkmcnt(0)
	s_cmpk_gt_i32 s61, 0xbff
	s_cbranch_scc1 .Lpf_dif_skip
	s_mul_hi_i32 s84, s61, 0x2aaaaaab
	s_lshr_b32 s84, s84, 4
	s_mul_i32 s85, s84, 0xffffffa0
	s_add_i32 s85, s85, s61
	v_readlane_b32 s87, v254, 7
	v_readlane_b32 s88, v253, 1
	v_readlane_b32 s89, v253, 2
	s_lshl_b32 s86, s61, 7
	s_and_b32 s86, s86, 0x380
	v_ashrrev_i32_e32 v246, 2, v0
	v_and_b32_e32 v246, -4, v246
	v_add_u32_e32 v246, s86, v246
	v_lshlrev_b32_e32 v248, 4, v0
	v_and_b32_e32 v248, 0xf0, v248
	s_lshl_b32 s87, s87, 5
	s_add_i32 s92, s84, s87
	s_mov_b32 s93, 0
	s_cmp_gt_i32 s85, 63
	s_cbranch_scc1 .Lpf_dif_w2
	s_load_dwordx2 s[90:91], s[88:89], 0xa0
	s_lshl_b64 s[92:93], s[92:93], 23
	v_lshlrev_b32_e32 v246, 13, v246
	s_lshl_b32 s86, s85, 4
	s_and_b32 s86, s86, 0xffffff80
	s_lshl_b32 s86, s86, 2
	v_add3_u32 v246, v246, v248, s86
	v_mov_b32_e32 v247, 0
	s_waitcnt lgkmcnt(0)
	s_add_u32 s90, s90, s92
	s_addc_u32 s91, s91, s93
	v_lshl_add_u64 v[246:247], s[90:91], 0, v[246:247]
	s_mov_b64 s[94:95], 0x2000
	v_lshl_add_u64 v[248:249], v[246:247], 0, s[94:95]
	global_load_dwordx4 v[148:151], v[248:249], off nt
	s_mov_b64 s[94:95], 0x4000
	v_lshl_add_u64 v[250:251], v[246:247], 0, s[94:95]
	global_load_dwordx4 v[168:171], v[250:251], off nt
	global_load_dwordx4 v[172:175], v[246:247], off nt
	global_load_dwordx4 v[176:179], v[246:247], off offset:256 nt
	s_mov_b64 s[94:95], 0x6000
	v_lshl_add_u64 v[248:249], v[246:247], 0, s[94:95]
	global_load_dwordx4 v[188:191], v[248:249], off nt
	s_mov_b64 s[94:95], 0x2000
	v_lshl_add_u64 v[250:251], v[246:247], 0, s[94:95]
	global_load_dwordx4 v[192:195], v[250:251], off offset:256 nt
	s_mov_b64 s[94:95], 0x4000
	v_lshl_add_u64 v[248:249], v[246:247], 0, s[94:95]
	global_load_dwordx4 v[202:205], v[248:249], off offset:256 nt
	s_mov_b64 s[94:95], 0x6000
	v_lshl_add_u64 v[250:251], v[246:247], 0, s[94:95]
	global_load_dwordx4 v[206:209], v[250:251], off offset:256 nt
	s_mov_b64 s[94:95], 0x1000
	v_lshl_add_u64 v[248:249], v[246:247], 0, s[94:95]
	global_load_dwordx4 v[210:213], v[248:249], off nt
	s_mov_b64 s[94:95], 0x3000
	v_lshl_add_u64 v[250:251], v[246:247], 0, s[94:95]
	global_load_dwordx4 v[214:217], v[250:251], off nt
	s_mov_b64 s[94:95], 0x5000
	v_lshl_add_u64 v[248:249], v[246:247], 0, s[94:95]
	global_load_dwordx4 v[222:225], v[248:249], off nt
	s_mov_b64 s[94:95], 0x7000
	v_lshl_add_u64 v[250:251], v[246:247], 0, s[94:95]
	global_load_dwordx4 v[226:229], v[250:251], off nt
	s_mov_b64 s[94:95], 0x1000
	v_lshl_add_u64 v[248:249], v[246:247], 0, s[94:95]
	global_load_dwordx4 v[230:233], v[248:249], off offset:256 nt
	s_mov_b64 s[94:95], 0x3000
	v_lshl_add_u64 v[250:251], v[246:247], 0, s[94:95]
	global_load_dwordx4 v[234:237], v[250:251], off offset:256 nt
	s_mov_b64 s[94:95], 0x5000
	v_lshl_add_u64 v[248:249], v[246:247], 0, s[94:95]
	global_load_dwordx4 v[238:241], v[248:249], off offset:256 nt
	s_mov_b64 s[94:95], 0x7000
	v_lshl_add_u64 v[250:251], v[246:247], 0, s[94:95]
	global_load_dwordx4 v[242:245], v[250:251], off offset:256 nt
	s_branch .Lpf_dif_skip
.Lpf_dif_w2:
	s_load_dwordx2 s[90:91], s[88:89], 0xb0
	s_lshl_b64 s[92:93], s[92:93], 22
	v_lshlrev_b32_e32 v246, 12, v246
	s_lshl_b32 s86, s85, 5
	s_and_b32 s86, s86, 0xffffff00
	s_add_i32 s86, s86, 0xfffff800
	s_lshl_b32 s86, s86, 2
	v_add3_u32 v246, v246, v248, s86
	v_mov_b32_e32 v247, 0
	s_waitcnt lgkmcnt(0)
	s_add_u32 s90, s90, s92
	s_addc_u32 s91, s91, s93
	v_lshl_add_u64 v[246:247], s[90:91], 0, v[246:247]
	s_mov_b64 s[94:95], 0x1000
	v_lshl_add_u64 v[248:249], v[246:247], 0, s[94:95]
	global_load_dwordx4 v[148:151], v[248:249], off nt
	s_mov_b64 s[94:95], 0x2000
	v_lshl_add_u64 v[250:251], v[246:247], 0, s[94:95]
	global_load_dwordx4 v[168:171], v[250:251], off nt
	global_load_dwordx4 v[172:175], v[246:247], off nt
	global_load_dwordx4 v[176:179], v[246:247], off offset:256 nt
	s_mov_b64 s[94:95], 0x3000
	v_lshl_add_u64 v[248:249], v[246:247], 0, s[94:95]
	global_load_dwordx4 v[188:191], v[248:249], off nt
	s_mov_b64 s[94:95], 0x1000
	v_lshl_add_u64 v[250:251], v[246:247], 0, s[94:95]
	global_load_dwordx4 v[192:195], v[250:251], off offset:256 nt
	s_mov_b64 s[94:95], 0x2000
	v_lshl_add_u64 v[248:249], v[246:247], 0, s[94:95]
	global_load_dwordx4 v[202:205], v[248:249], off offset:256 nt
	s_mov_b64 s[94:95], 0x3000
	v_lshl_add_u64 v[250:251], v[246:247], 0, s[94:95]
	global_load_dwordx4 v[206:209], v[250:251], off offset:256 nt
	global_load_dwordx4 v[210:213], v[246:247], off offset:512 nt
	s_mov_b64 s[94:95], 0x1000
	v_lshl_add_u64 v[248:249], v[246:247], 0, s[94:95]
	global_load_dwordx4 v[214:217], v[248:249], off offset:512 nt
	s_mov_b64 s[94:95], 0x2000
	v_lshl_add_u64 v[250:251], v[246:247], 0, s[94:95]
	global_load_dwordx4 v[222:225], v[250:251], off offset:512 nt
	s_mov_b64 s[94:95], 0x3000
	v_lshl_add_u64 v[248:249], v[246:247], 0, s[94:95]
	global_load_dwordx4 v[226:229], v[248:249], off offset:512 nt
	global_load_dwordx4 v[230:233], v[246:247], off offset:768 nt
	s_mov_b64 s[94:95], 0x1000
	v_lshl_add_u64 v[250:251], v[246:247], 0, s[94:95]
	global_load_dwordx4 v[234:237], v[250:251], off offset:768 nt
	s_mov_b64 s[94:95], 0x2000
	v_lshl_add_u64 v[248:249], v[246:247], 0, s[94:95]
	global_load_dwordx4 v[238:241], v[248:249], off offset:768 nt
	s_mov_b64 s[94:95], 0x3000
	v_lshl_add_u64 v[250:251], v[246:247], 0, s[94:95]
	global_load_dwordx4 v[242:245], v[250:251], off offset:768 nt
.Lpf_dif_skip:
	v_fma_f32 v70, -v4, v5, 1.0
	v_fmac_f32_e32 v5, v70, v5
	v_div_scale_f32 v70, vcc, 1.0, v2, 1.0
	v_mul_f32_e32 v71, v70, v5
	v_fma_f32 v72, -v4, v71, v70
	v_fmac_f32_e32 v71, v72, v5
	v_fma_f32 v4, -v4, v71, v70
	v_div_fmas_f32 v4, v4, v5, v71
	v_div_fixup_f32 v142, v4, v2, 1.0
	v_or_b32_e32 v2, s4, v159
	s_movk_i32 s4, 0x210
	s_and_b64 vcc, exec, s[2:3]
	v_mul_lo_u32 v2, v2, s4
	s_barrier
	s_cbranch_vccnz .LBB0_464
	v_add3_u32 v4, 0, v2, v144
	v_pk_mul_f32 v[70:71], v[54:55], v[142:143] op_sel_hi:[1,0]
	v_pk_mul_f32 v[72:73], v[56:57], v[142:143] op_sel_hi:[1,0]
	ds_write_b128 v4, v[70:73]
	v_pk_mul_f32 v[70:71], v[58:59], v[142:143] op_sel_hi:[1,0]
	v_pk_mul_f32 v[72:73], v[60:61], v[142:143] op_sel_hi:[1,0]
	ds_write_b128 v4, v[70:73] offset:32
	v_pk_mul_f32 v[70:71], v[62:63], v[142:143] op_sel_hi:[1,0]
	v_pk_mul_f32 v[72:73], v[64:65], v[142:143] op_sel_hi:[1,0]
	ds_write_b128 v4, v[70:73] offset:64
	v_pk_mul_f32 v[70:71], v[66:67], v[142:143] op_sel_hi:[1,0]
	v_pk_mul_f32 v[72:73], v[68:69], v[142:143] op_sel_hi:[1,0]
	ds_write_b128 v4, v[70:73] offset:96
	v_pk_mul_f32 v[70:71], v[38:39], v[142:143] op_sel_hi:[1,0]
	v_pk_mul_f32 v[72:73], v[40:41], v[142:143] op_sel_hi:[1,0]
	ds_write_b128 v4, v[70:73] offset:128
	v_pk_mul_f32 v[70:71], v[42:43], v[142:143] op_sel_hi:[1,0]
	v_pk_mul_f32 v[72:73], v[44:45], v[142:143] op_sel_hi:[1,0]
	ds_write_b128 v4, v[70:73] offset:160
	v_pk_mul_f32 v[70:71], v[46:47], v[142:143] op_sel_hi:[1,0]
	v_pk_mul_f32 v[72:73], v[48:49], v[142:143] op_sel_hi:[1,0]
	ds_write_b128 v4, v[70:73] offset:192
	v_pk_mul_f32 v[70:71], v[50:51], v[142:143] op_sel_hi:[1,0]
	v_pk_mul_f32 v[72:73], v[52:53], v[142:143] op_sel_hi:[1,0]
	ds_write_b128 v4, v[70:73] offset:224
	v_pk_mul_f32 v[70:71], v[22:23], v[142:143] op_sel_hi:[1,0]
	v_pk_mul_f32 v[72:73], v[24:25], v[142:143] op_sel_hi:[1,0]
	ds_write_b128 v4, v[70:73] offset:256
	v_pk_mul_f32 v[70:71], v[26:27], v[142:143] op_sel_hi:[1,0]
	v_pk_mul_f32 v[72:73], v[28:29], v[142:143] op_sel_hi:[1,0]
	ds_write_b128 v4, v[70:73] offset:288
	v_pk_mul_f32 v[70:71], v[30:31], v[142:143] op_sel_hi:[1,0]
	v_pk_mul_f32 v[72:73], v[32:33], v[142:143] op_sel_hi:[1,0]
	ds_write_b128 v4, v[70:73] offset:320
	v_pk_mul_f32 v[70:71], v[34:35], v[142:143] op_sel_hi:[1,0]
	v_pk_mul_f32 v[72:73], v[36:37], v[142:143] op_sel_hi:[1,0]
	ds_write_b128 v4, v[70:73] offset:352
	v_pk_mul_f32 v[70:71], v[6:7], v[142:143] op_sel_hi:[1,0]
	v_pk_mul_f32 v[72:73], v[8:9], v[142:143] op_sel_hi:[1,0]
	ds_write_b128 v4, v[70:73] offset:384
	v_pk_mul_f32 v[70:71], v[10:11], v[142:143] op_sel_hi:[1,0]
	v_pk_mul_f32 v[72:73], v[12:13], v[142:143] op_sel_hi:[1,0]
	ds_write_b128 v4, v[70:73] offset:416
	v_pk_mul_f32 v[70:71], v[14:15], v[142:143] op_sel_hi:[1,0]
	v_pk_mul_f32 v[72:73], v[16:17], v[142:143] op_sel_hi:[1,0]
	ds_write_b128 v4, v[70:73] offset:448
	v_pk_mul_f32 v[70:71], v[18:19], v[142:143] op_sel_hi:[1,0]
	v_pk_mul_f32 v[72:73], v[20:21], v[142:143] op_sel_hi:[1,0]
	ds_write_b128 v4, v[70:73] offset:480

.LBB0_478:
	v_lshlrev_b32_e32 v36, 4, v38
	v_and_b32_e32 v2, 0xf0, v36
	v_lshl_add_u64 v[28:29], v[4:5], 0, v[2:3]
	v_lshl_add_u64 v[4:5], v[28:29], 0, s[48:49]
	v_lshl_add_u64 v[6:7], v[28:29], 0, s[46:47]
	s_waitcnt vmcnt(0)
	v_mov_b32_e32 v40, v148
	v_mov_b32_e32 v41, v149
	v_mov_b32_e32 v42, v150
	v_mov_b32_e32 v43, v151
	v_mov_b32_e32 v44, v168
	v_mov_b32_e32 v45, v169
	v_mov_b32_e32 v46, v170
	v_mov_b32_e32 v47, v171
	v_lshl_add_u64 v[4:5], v[28:29], 0, s[44:45]
	v_mov_b32_e32 v84, v172
	v_mov_b32_e32 v85, v173
	v_mov_b32_e32 v86, v174
	v_mov_b32_e32 v87, v175
	v_mov_b32_e32 v66, v176
	v_mov_b32_e32 v67, v177
	v_mov_b32_e32 v68, v178
	v_mov_b32_e32 v69, v179
	v_lshl_add_u64 v[6:7], v[28:29], 0, s[42:43]
	v_mov_b32_e32 v76, v188
	v_mov_b32_e32 v77, v189
	v_mov_b32_e32 v78, v190
	v_mov_b32_e32 v79, v191
	v_mov_b32_e32 v70, v192
	v_mov_b32_e32 v71, v193
	v_mov_b32_e32 v72, v194
	v_mov_b32_e32 v73, v195
	v_lshl_add_u64 v[4:5], v[28:29], 0, s[40:41]
	v_lshl_add_u64 v[6:7], v[28:29], 0, s[38:39]
	v_mov_b32_e32 v60, v202
	v_mov_b32_e32 v61, v203
	v_mov_b32_e32 v62, v204
	v_mov_b32_e32 v63, v205
	v_mov_b32_e32 v88, v206
	v_mov_b32_e32 v89, v207
	v_mov_b32_e32 v90, v208
	v_mov_b32_e32 v91, v209
	v_lshl_add_u64 v[4:5], v[28:29], 0, s[36:37]
	v_lshl_add_u64 v[8:9], v[28:29], 0, s[30:31]
	v_lshl_add_u64 v[12:13], v[28:29], 0, s[28:29]
	v_lshl_add_u64 v[16:17], v[28:29], 0, s[26:27]
	v_lshl_add_u64 v[20:21], v[28:29], 0, s[22:23]
	v_lshl_add_u64 v[24:25], v[28:29], 0, s[18:19]
	v_lshl_add_u64 v[30:31], v[28:29], 0, s[16:17]
	v_lshl_add_u64 v[32:33], v[28:29], 0, s[14:15]
	v_mov_b32_e32 v4, v210
	v_mov_b32_e32 v5, v211
	v_mov_b32_e32 v6, v212
	v_mov_b32_e32 v7, v213
	v_mov_b32_e32 v8, v214
	v_mov_b32_e32 v9, v215
	v_mov_b32_e32 v10, v216
	v_mov_b32_e32 v11, v217
	v_mov_b32_e32 v12, v222
	v_mov_b32_e32 v13, v223
	v_mov_b32_e32 v14, v224
	v_mov_b32_e32 v15, v225
	v_mov_b32_e32 v16, v226
	v_mov_b32_e32 v17, v227
	v_mov_b32_e32 v18, v228
	v_mov_b32_e32 v19, v229
	v_mov_b32_e32 v20, v230
	v_mov_b32_e32 v21, v231
	v_mov_b32_e32 v22, v232
	v_mov_b32_e32 v23, v233
	v_mov_b32_e32 v24, v234
	v_mov_b32_e32 v25, v235
	v_mov_b32_e32 v26, v236
	v_mov_b32_e32 v27, v237
	v_mov_b32_e32 v28, v238
	v_mov_b32_e32 v29, v239
	v_mov_b32_e32 v30, v240
	v_mov_b32_e32 v31, v241
	v_mov_b32_e32 v32, v242
	v_mov_b32_e32 v33, v243
	v_mov_b32_e32 v34, v244
	v_mov_b32_e32 v35, v245
	v_ashrrev_i32_e32 v39, 6, v38
	v_lshlrev_b32_e32 v37, 9, v38
	v_bitop3_b32 v39, v39, v38, 7 bitop3:0x78
	v_lshrrev_b32_e32 v2, 2, v38
	v_and_b32_e32 v37, 0x1e00, v37
	v_lshlrev_b32_e32 v39, 4, v39
	v_add3_u32 v39, 0, v37, v39
	v_and_b32_e32 v48, 12, v2
	v_ashrrev_i32_e32 v37, 3, v38
	v_lshrrev_b32_e32 v49, 5, v38
	v_add_u32_e32 v48, v39, v48
	v_and_b32_e32 v2, 0x70, v36
	v_add_u32_e32 v36, s50, v37
	s_mov_b64 s[14:15], -1
	s_and_b64 vcc, exec, s[2:3]
	v_lshlrev_b32_e32 v37, 7, v37
	v_xor_b32_e32 v82, v49, v38
	v_mul_f32_e32 v49, 0x42000000, v91
	v_mul_f32_e32 v50, 0x42000000, v63
	v_mul_f32_e32 v52, 0x42000000, v73
	v_mul_f32_e32 v54, 0x42000000, v69
	v_mul_f32_e32 v51, 0x42000000, v90
	v_mul_f32_e32 v53, 0x42000000, v62
	v_mul_f32_e32 v57, 0x42000000, v72
	v_mul_f32_e32 v58, 0x42000000, v68
	v_mul_f32_e32 v55, 0x42000000, v89
	v_mul_f32_e32 v56, 0x42000000, v61
	v_mul_f32_e32 v61, 0x42000000, v71
	v_mul_f32_e32 v62, 0x42000000, v67
	v_mul_f32_e32 v59, 0x42000000, v88
	v_mul_f32_e32 v60, 0x42000000, v60
	v_mul_f32_e32 v64, 0x42000000, v70
	v_mul_f32_e32 v65, 0x42000000, v66
	v_mul_f32_e32 v66, 0x42000000, v79
	v_mul_f32_e32 v67, 0x42000000, v47
	v_mul_f32_e32 v69, 0x42000000, v43
	v_mul_f32_e32 v71, 0x42000000, v87
	v_mul_f32_e32 v68, 0x42000000, v78
	v_mul_f32_e32 v70, 0x42000000, v46
	v_mul_f32_e32 v74, 0x42000000, v42
	v_mul_f32_e32 v75, 0x42000000, v86
	v_mul_f32_e32 v72, 0x42000000, v77
	v_mul_f32_e32 v73, 0x42000000, v45
	v_mul_f32_e32 v78, 0x42000000, v41
	v_mul_f32_e32 v79, 0x42000000, v85
	v_mul_f32_e32 v76, 0x42000000, v76
	v_mul_f32_e32 v77, 0x42000000, v44
	v_mul_f32_e32 v80, 0x42000000, v40
	v_mul_f32_e32 v81, 0x42000000, v84
	v_add_u32_e32 v63, 0x2000, v48
	v_add_u32_e32 v47, 0x4000, v48
	v_add_u32_e32 v46, 0x6000, v48
	s_barrier
	s_cbranch_vccz .LBB0_480
	v_mov_b32_e32 v116, v3
	v_mov_b32_e32 v117, v3
	v_cvt_pk_fp8_f32 v116, v81, v80
	v_cvt_pk_fp8_f32 v117, v79, v78
	v_mul_f32_e32 v114, 0x42000000, v8
	v_mul_f32_e32 v115, 0x42000000, v4
	v_cvt_pk_fp8_f32 v116, v77, v76 op_sel:[0,0,1]
	v_cvt_pk_fp8_f32 v117, v73, v72 op_sel:[0,0,1]
	v_mul_f32_e32 v112, 0x42000000, v16
	v_mul_f32_e32 v113, 0x42000000, v12
	v_mul_f32_e32 v110, 0x42000000, v9
	ds_write2_b32 v48, v116, v117 offset1:32
	v_mov_b32_e32 v116, v3
	v_mov_b32_e32 v117, v3
	v_cvt_pk_fp8_f32 v116, v75, v74
	v_cvt_pk_fp8_f32 v117, v71, v69
	v_mul_f32_e32 v111, 0x42000000, v5
	v_mul_f32_e32 v108, 0x42000000, v17
	v_cvt_pk_fp8_f32 v116, v70, v68 op_sel:[0,0,1]
	v_cvt_pk_fp8_f32 v117, v67, v66 op_sel:[0,0,1]
	v_mul_f32_e32 v109, 0x42000000, v13
	v_mul_f32_e32 v106, 0x42000000, v10
	v_mul_f32_e32 v107, 0x42000000, v6
	ds_write2_b32 v48, v116, v117 offset0:64 offset1:96
	v_mov_b32_e32 v116, v3
	v_mov_b32_e32 v117, v3
	v_cvt_pk_fp8_f32 v116, v65, v64
	v_cvt_pk_fp8_f32 v117, v62, v61
	v_mul_f32_e32 v104, 0x42000000, v18
	v_mul_f32_e32 v105, 0x42000000, v14
	v_cvt_pk_fp8_f32 v116, v60, v59 op_sel:[0,0,1]
	v_cvt_pk_fp8_f32 v117, v56, v55 op_sel:[0,0,1]
	v_mul_f32_e32 v102, 0x42000000, v11
	v_mul_f32_e32 v103, 0x42000000, v7
	v_mul_f32_e32 v100, 0x42000000, v19
	ds_write2_b32 v63, v116, v117 offset1:32
	v_mov_b32_e32 v116, v3
	v_mov_b32_e32 v117, v3
	v_cvt_pk_fp8_f32 v116, v58, v57
	v_cvt_pk_fp8_f32 v117, v54, v52
	v_mul_f32_e32 v101, 0x42000000, v15
	v_mul_f32_e32 v98, 0x42000000, v24
	v_cvt_pk_fp8_f32 v116, v53, v51 op_sel:[0,0,1]
	v_cvt_pk_fp8_f32 v117, v50, v49 op_sel:[0,0,1]
	v_mul_f32_e32 v99, 0x42000000, v20
	v_mul_f32_e32 v96, 0x42000000, v32
	v_mul_f32_e32 v97, 0x42000000, v28
	ds_write2_b32 v63, v116, v117 offset0:64 offset1:96
	v_mov_b32_e32 v116, v3
	v_cvt_pk_fp8_f32 v116, v115, v114
	v_mul_f32_e32 v94, 0x42000000, v25
	v_mul_f32_e32 v95, 0x42000000, v21
	v_mul_f32_e32 v92, 0x42000000, v33
	v_cvt_pk_fp8_f32 v116, v113, v112 op_sel:[0,0,1]
	v_mov_b32_e32 v112, v3
	v_cvt_pk_fp8_f32 v112, v111, v110
	v_mul_f32_e32 v93, 0x42000000, v29
	v_mul_f32_e32 v90, 0x42000000, v26
	v_mul_f32_e32 v91, 0x42000000, v22
	v_cvt_pk_fp8_f32 v112, v109, v108 op_sel:[0,0,1]
	v_mov_b32_e32 v108, v3
	v_cvt_pk_fp8_f32 v108, v107, v106
	s_lshl_b64 s[2:3], s[4:5], 20
	s_add_u32 s2, s56, s2
	v_lshlrev_b32_e32 v40, 4, v82
	v_cvt_pk_fp8_f32 v108, v105, v104 op_sel:[0,0,1]
	v_mov_b32_e32 v104, v3
	v_cvt_pk_fp8_f32 v104, v103, v102
	v_mul_f32_e32 v88, 0x42000000, v34
	v_mul_f32_e32 v89, 0x42000000, v30
	s_addc_u32 s3, s57, s3
	v_cvt_pk_fp8_f32 v104, v101, v100 op_sel:[0,0,1]
	v_mov_b32_e32 v100, v3
	v_cvt_pk_fp8_f32 v100, v99, v98
	v_and_b32_e32 v40, 0x70, v40
	v_mul_f32_e32 v86, 0x42000000, v27
	v_mul_f32_e32 v87, 0x42000000, v23
	v_cvt_pk_fp8_f32 v100, v97, v96 op_sel:[0,0,1]
	v_mov_b32_e32 v96, v3
	v_cvt_pk_fp8_f32 v96, v95, v94
	s_add_u32 s2, s2, s33
	v_add_u32_e32 v84, 0xfffff800, v36
	v_add_u32_e32 v38, 0xfffff8c0, v36
	v_cvt_pk_fp8_f32 v96, v93, v92 op_sel:[0,0,1]
	v_mov_b32_e32 v92, v3
	v_cvt_pk_fp8_f32 v92, v91, v90
	v_add3_u32 v83, 0, v37, v40
	v_add_u32_e32 v40, 0xfffff880, v36
	v_add_u32_e32 v42, 0xfffff840, v36
	v_cvt_pk_fp8_f32 v92, v89, v88 op_sel:[0,0,1]
	v_mov_b32_e32 v88, v3
	v_cvt_pk_fp8_f32 v88, v87, v86
	s_addc_u32 s3, s3, 0
	v_ashrrev_i32_e32 v39, 31, v38
	v_ashrrev_i32_e32 v41, 31, v40
	v_ashrrev_i32_e32 v43, 31, v42
	v_ashrrev_i32_e32 v85, 31, v84
	v_lshl_add_u64 v[44:45], s[2:3], 0, v[2:3]
	v_lshlrev_b64 v[38:39], 10, v[38:39]
	v_lshlrev_b64 v[40:41], 10, v[40:41]
	v_lshlrev_b64 v[42:43], 10, v[42:43]
	v_lshlrev_b64 v[84:85], 10, v[84:85]
	v_lshl_add_u64 v[38:39], v[44:45], 0, v[38:39]
	v_lshl_add_u64 v[40:41], v[44:45], 0, v[40:41]
	v_lshl_add_u64 v[42:43], v[44:45], 0, v[42:43]
	v_lshl_add_u64 v[44:45], v[44:45], 0, v[84:85]
	v_mul_f32_e32 v84, 0x42000000, v35
	v_mul_f32_e32 v85, 0x42000000, v31
	v_cvt_pk_fp8_f32 v88, v85, v84 op_sel:[0,0,1]
	ds_write2_b32 v47, v116, v112 offset1:32
	ds_write2_b32 v47, v108, v104 offset0:64 offset1:96
	ds_write2_b32 v46, v100, v96 offset1:32
	ds_write2_b32 v46, v92, v88 offset0:64 offset1:96
	s_waitcnt lgkmcnt(0)
	s_barrier
	ds_read_b128 v[84:87], v83
	s_mov_b64 s[14:15], 0
	s_waitcnt lgkmcnt(0)
	global_store_dwordx4 v[44:45], v[84:87], off
	ds_read_b128 v[84:87], v83 offset:8192
	s_waitcnt lgkmcnt(0)
	global_store_dwordx4 v[42:43], v[84:87], off
	ds_read_b128 v[42:45], v83 offset:16384
	s_waitcnt lgkmcnt(0)
	global_store_dwordx4 v[40:41], v[42:45], off
	ds_read_b128 v[40:43], v83 offset:24576
	s_waitcnt lgkmcnt(0)
	global_store_dwordx4 v[38:39], v[40:43], off
	s_barrier
